# hd1: attention tile loops: each tile leads with its first QK^T MFMA (wait + MFMA moved ahead of the two v_exp / two v_add of the previous tile's tail); on top of cv1
# baseline (speedup 1.0000x reference)
; #define SBAR() __builtin_amdgcn_sched_barrier(0)
; #define SLOAD(k0) do { vs0 = *reinterpret_cast<const bf16x8*>(&Vh[(size_t)((k0) + sr) * DM + sc]); vs1 = *reinterpret_cast<const bf16x8*>(&Vh[(size_t)((k0) + 32 + sr) * DM + sc]); \
;     ks = *reinterpret_cast<const bf16x8*>(&Kh[(size_t)((k0) + kr) * DM + kc]); } while (0)
; #define SWRITE(s) do { *(bf16x8*)(V_lds + (s) * SHM_V + vst0) = vs0; *(bf16x8*)(V_lds + (s) * SHM_V + vst1) = vs1; *(bf16x8*)(K_lds + (s) * SHM_K64 + kst) = ks; } while (0)
; #define RESC(a) do { if (__any((a) < 1.f)) { if (hi == 0) al_l[r32] = (a); asm volatile("s_waitcnt lgkmcnt(0)" ::: "memory"); \
;     _Pragma("unroll") for (int d = 0; d < 4; ++d) _Pragma("unroll") for (int r = 0; r < 16; ++r) o[d][r] *= al_l[crow(r, hi)]; } } while (0)
; #define ROT() do { s_prev = s_cur; s_cur = s_next; s_next = (s_next == DA_NBUF - 1) ? 0 : s_next + 1; } while (0)
; __device__ __forceinline__ void diff_pass(const bf16_t* __restrict__ Qb, const bf16_t* __restrict__ Kh, const bf16_t* __restrict__ Vh, int seq, char* lds, f32x16 (&o)[4], const int wave_) {
;     ...
;     for (int j = 1; j + 1 < NT; j += 2) {
;         SLOAD((j + 1) * 64);
;         SBAR(); qkt64c(pB0, pB1, K_lds + s_cur * SHM_K64, qr, negm, r32, hi); FIN(pA0, pA1, alA); SBAR();
;         YSEG(pB0, pB1, alB, s_prev);
;         SWRITE(s_next); RESC(alB); __syncthreads(); ROT();
;         SLOAD((j + 2) * 64);
;         SBAR(); qkt64c(pA0, pA1, K_lds + s_cur * SHM_K64, qr, negm, r32, hi); FIN(pB0, pB1, alB); SBAR();
;         YSEG(pA0, pA1, alA, s_prev);
.Latt9_p1_top:
	ds_read_b128 v[144:147], v128 offset:49152
	ds_read_b128 v[148:151], v129 offset:49152
	ds_read_b128 v[152:155], v130 offset:49152
	ds_read_b128 v[156:159], v131 offset:49152
	ds_read_b128 v[232:235], v128 offset:53248
	ds_read_b128 v[236:239], v129 offset:53248
	ds_read_b128 v[240:243], v130 offset:53248
	ds_read_b128 v[244:247], v131 offset:53248
	s_lshl_b32 s19, s41, 14
	s_add_i32 s19, s19, s18
	s_mov_b32 m0, s19
	s_lshl_b32 s20, s41, 13
	global_load_lds_dwordx4 v195, s[16:17]
	s_add_i32 m0, s19, 0x2000
	s_add_i32 s20, s20, s18
	global_load_lds_dwordx4 v255, s[16:17]
	s_add_i32 m0, s20, 0xc000
	s_add_u32 s16, s16, 0x20000
	global_load_lds_dwordx4 v194, s[14:15]
	s_addc_u32 s17, s17, 0
	s_add_u32 s14, s14, 0x20000
	s_addc_u32 s15, s15, 0
	s_waitcnt lgkmcnt(7)
	v_mfma_f32_32x32x16_bf16 v[128:143], v[144:147], v[162:165], v[80:95]
	v_exp_f32_e32 v190, v120
	v_exp_f32_e32 v191, v121
	v_add_f32_e32 v120, v96, v97
	v_add_f32_e32 v121, v98, v99
	v_exp_f32_e32 v192, v122
	v_add_f32_e32 v120, v120, v121
	v_add_f32_e32 v121, v100, v101
	v_add_f32_e32 v122, v102, v103
	v_exp_f32_e32 v193, v123
	s_waitcnt lgkmcnt(6)
	v_mfma_f32_32x32x16_bf16 v[128:143], v[148:151], v[166:169], v[128:143]
	v_add_f32_e32 v121, v121, v122
	v_add_f32_e32 v122, v104, v105
	v_add_f32_e32 v123, v106, v107
	v_add_f32_e32 v122, v122, v123
	v_add_f32_e32 v123, v108, v109
	s_waitcnt lgkmcnt(5)
	v_mfma_f32_32x32x16_bf16 v[128:143], v[152:155], v[170:173], v[128:143]
	v_add_f32_e32 v208, v110, v111
	v_add_f32_e32 v123, v123, v208
	v_add_f32_e32 v208, v112, v113
	v_add_f32_e32 v209, v114, v115
	v_add_f32_e32 v208, v208, v209
	s_waitcnt lgkmcnt(4)
	v_mfma_f32_32x32x16_bf16 v[128:143], v[156:159], v[174:177], v[128:143]
	v_exp_f32_e32 v124, v124
	v_exp_f32_e32 v125, v125
	s_waitcnt lgkmcnt(3)
	v_mfma_f32_32x32x16_bf16 v[144:159], v[232:235], v[162:165], v[80:95]
	v_lshl_add_u32 v234, s12, 14, v217
	ds_read_b64_tr_b16 v[64:65], v234 offset:0
	ds_read_b64_tr_b16 v[66:67], v234 offset:0x800
	ds_read_b64_tr_b16 v[68:69], v234 offset:0x1000
	ds_read_b64_tr_b16 v[70:71], v234 offset:0x1800
	ds_read_b64_tr_b16 v[72:73], v234 offset:0x2000
	ds_read_b64_tr_b16 v[74:75], v234 offset:0x2800
	ds_read_b64_tr_b16 v[76:77], v234 offset:0x3000
	ds_read_b64_tr_b16 v[78:79], v234 offset:0x3800
	v_exp_f32_e32 v126, v126
	v_exp_f32_e32 v127, v127
	v_add_f32_e32 v120, v208, v120
	v_add_f32_e32 v208, v116, v117
	v_add_f32_e32 v209, v118, v119
	v_add_f32_e32 v208, v208, v209
	v_add_f32_e32 v121, v208, v121
	s_waitcnt lgkmcnt(10)
	v_mfma_f32_32x32x16_bf16 v[144:159], v[236:239], v[166:169], v[144:159]
	v_add_f32_e32 v208, v190, v191
	v_add_f32_e32 v209, v192, v193
	v_add_f32_e32 v208, v208, v209
	v_add_f32_e32 v122, v122, v208
	v_add_f32_e32 v208, v124, v125
	v_add_f32_e32 v209, v126, v127
	v_add_f32_e32 v208, v208, v209
	s_waitcnt lgkmcnt(9)
	v_mfma_f32_32x32x16_bf16 v[144:159], v[240:243], v[170:173], v[144:159]
	v_add_f32_e32 v123, v123, v208
	v_add_f32_e32 v120, v120, v121
	v_add_f32_e32 v121, v122, v123
	v_add_f32_e32 v231, v120, v121
	v_mov_b32_e32 v232, v231
	v_cvt_pk_bf16_f32 v96, v96, v97
	v_cvt_pk_bf16_f32 v97, v98, v99
	s_waitcnt lgkmcnt(8)
	v_mfma_f32_32x32x16_bf16 v[144:159], v[244:247], v[174:177], v[144:159]
	v_cvt_pk_bf16_f32 v98, v100, v101
	v_cvt_pk_bf16_f32 v99, v102, v103
	v_cvt_pk_bf16_f32 v120, v104, v105
	v_cvt_pk_bf16_f32 v121, v106, v107
	v_cvt_pk_bf16_f32 v122, v108, v109
	v_cvt_pk_bf16_f32 v123, v110, v111
	v_permlane32_swap_b32_e32 v96, v98
	v_permlane32_swap_b32_e32 v97, v99
	v_cvt_pk_bf16_f32 v104, v112, v113
	v_cvt_pk_bf16_f32 v105, v114, v115
	v_cvt_pk_bf16_f32 v106, v116, v117
	v_cvt_pk_bf16_f32 v107, v118, v119
	s_waitcnt lgkmcnt(0)
	v_mfma_f32_32x32x16_bf16 v[0:15], v[96:99], v[64:67], v[0:15]
	v_permlane32_swap_b32_e32 v120, v122
	v_permlane32_swap_b32_e32 v121, v123
	v_cvt_pk_bf16_f32 v100, v190, v191
	v_cvt_pk_bf16_f32 v101, v192, v193
	v_cvt_pk_bf16_f32 v102, v124, v125
	v_cvt_pk_bf16_f32 v103, v126, v127
	v_mfma_f32_32x32x16_bf16 v[0:15], v[120:123], v[68:71], v[0:15]
	v_permlane32_swap_b32_e32 v104, v106
	v_permlane32_swap_b32_e32 v105, v107
	ds_read_b64_tr_b16 v[236:237], v234 offset:0x200
	ds_read_b64_tr_b16 v[238:239], v234 offset:0xa00
	ds_read_b64_tr_b16 v[240:241], v234 offset:0x1200
	ds_read_b64_tr_b16 v[242:243], v234 offset:0x1a00
	ds_read_b64_tr_b16 v[244:245], v234 offset:0x2200
	ds_read_b64_tr_b16 v[246:247], v234 offset:0x2a00
	ds_read_b64_tr_b16 v[190:191], v234 offset:0x3200
	ds_read_b64_tr_b16 v[192:193], v234 offset:0x3a00
	v_mfma_f32_32x32x16_bf16 v[0:15], v[104:107], v[72:75], v[0:15]
	v_permlane32_swap_b32_e32 v100, v102
	v_permlane32_swap_b32_e32 v101, v103
	v_permlane32_swap_b32_e32 v231, v232
	v_max_f32_e32 v108, v128, v129
	v_max3_f32 v109, v130, v131, v145
	v_max3_f32 v108, v108, v144, v146
	v_max3_f32 v108, v108, v147, v132
	v_max3_f32 v109, v109, v134, v135
	v_mfma_f32_32x32x16_bf16 v[0:15], v[100:103], v[76:79], v[0:15]
	v_max3_f32 v208, v108, v133, v148
	v_max3_f32 v209, v109, v150, v151
	ds_read_b64_tr_b16 v[124:125], v234 offset:0x400
	ds_read_b64_tr_b16 v[126:127], v234 offset:0xc00
	ds_read_b64_tr_b16 v[116:117], v234 offset:0x1400
	ds_read_b64_tr_b16 v[118:119], v234 offset:0x1c00
	ds_read_b64_tr_b16 v[112:113], v234 offset:0x2400
	ds_read_b64_tr_b16 v[114:115], v234 offset:0x2c00
	ds_read_b64_tr_b16 v[108:109], v234 offset:0x3400
	ds_read_b64_tr_b16 v[110:111], v234 offset:0x3c00
	s_waitcnt lgkmcnt(8)
	v_mfma_f32_32x32x16_bf16 v[48:63], v[96:99], v[236:239], v[48:63]
	v_max3_f32 v208, v208, v149, v136
	v_max3_f32 v209, v209, v138, v139
	v_max3_f32 v208, v208, v137, v152
	v_max3_f32 v209, v209, v154, v155
	v_max3_f32 v208, v208, v153, v140
	v_max3_f32 v209, v209, v142, v143
	v_max3_f32 v208, v208, v141, v156
	v_mfma_f32_32x32x16_bf16 v[48:63], v[120:123], v[240:243], v[48:63]
	v_max3_f32 v209, v209, v158, v159
	v_max3_f32 v208, v208, v157, v209
	v_mov_b32_e32 v209, v208
	s_nop 1
	v_permlane32_swap_b32_e32 v208, v209
	v_mfma_f32_32x32x16_bf16 v[48:63], v[104:107], v[244:247], v[48:63]
	v_max_f32_e32 v233, v208, v209
	s_mov_b32 s2, 0x4138aa3b
	v_cmp_ge_f32_e32 vcc, s2, v233
	v_mfma_f32_32x32x16_bf16 v[48:63], v[100:103], v[190:193], v[48:63]
	s_cmp_eq_u64 vcc, exec
	s_cbranch_scc0 .LBB0_836
	v_mov_b32_e32 v233, 1.0

; #define SBAR() __builtin_amdgcn_sched_barrier(0)
; #define SLOAD(k0) do { vs0 = *reinterpret_cast<const bf16x8*>(&Vh[(size_t)((k0) + sr) * DM + sc]); vs1 = *reinterpret_cast<const bf16x8*>(&Vh[(size_t)((k0) + 32 + sr) * DM + sc]); \
;     ks = *reinterpret_cast<const bf16x8*>(&Kh[(size_t)((k0) + kr) * DM + kc]); } while (0)
; #define SWRITE(s) do { *(bf16x8*)(V_lds + (s) * SHM_V + vst0) = vs0; *(bf16x8*)(V_lds + (s) * SHM_V + vst1) = vs1; *(bf16x8*)(K_lds + (s) * SHM_K64 + kst) = ks; } while (0)
; #define RESC(a) do { if (__any((a) < 1.f)) { if (hi == 0) al_l[r32] = (a); asm volatile("s_waitcnt lgkmcnt(0)" ::: "memory"); \
;     _Pragma("unroll") for (int d = 0; d < 4; ++d) _Pragma("unroll") for (int r = 0; r < 16; ++r) o[d][r] *= al_l[crow(r, hi)]; } } while (0)
; #define ROT() do { s_prev = s_cur; s_cur = s_next; s_next = (s_next == DA_NBUF - 1) ? 0 : s_next + 1; } while (0)
; __device__ __forceinline__ void diff_pass(const bf16_t* __restrict__ Qb, const bf16_t* __restrict__ Kh, const bf16_t* __restrict__ Vh, int seq, char* lds, f32x16 (&o)[4], const int wave_) {
;     ...
;     for (int j = 1; j + 1 < NT; j += 2) {
;         SLOAD((j + 1) * 64);
;         SBAR(); qkt64c(pB0, pB1, K_lds + s_cur * SHM_K64, qr, negm, r32, hi); FIN(pA0, pA1, alA); SBAR();
;         YSEG(pB0, pB1, alB, s_prev);
;         SWRITE(s_next); RESC(alB); __syncthreads(); ROT();
;         SLOAD((j + 2) * 64);
;         SBAR(); qkt64c(pA0, pA1, K_lds + s_cur * SHM_K64, qr, negm, r32, hi); FIN(pB0, pB1, alB); SBAR();
;         YSEG(pA0, pA1, alA, s_prev);
.LBB0_829:
	s_waitcnt lgkmcnt(0)
	v_add_u32_e32 v102, s2, v223
	v_add_u32_e32 v103, s2, v226
	v_add_u32_e32 v104, s2, v228
	v_add_u32_e32 v105, s2, v229
	s_waitcnt vmcnt(0)
	s_barrier
	ds_read_b128 v[112:115], v102 offset:49152
	ds_read_b128 v[116:119], v103 offset:49152
	ds_read_b128 v[120:123], v104 offset:49152
	ds_read_b128 v[124:127], v105 offset:49152
	ds_read_b128 v[190:193], v102 offset:53248
	ds_read_b128 v[202:205], v103 offset:53248
	ds_read_b128 v[234:237], v104 offset:53248
	ds_read_b128 v[238:241], v105 offset:53248
	s_add_i32 s3, s41, 1
	s_cmp_lg_u32 s41, 2
	s_cselect_b32 s3, s3, 0
	s_lshl_b32 s19, s3, 14
	s_add_i32 s19, s19, s18
	s_mov_b32 m0, s19
	s_lshl_b32 s20, s3, 13
	global_load_lds_dwordx4 v195, s[16:17]
	s_add_i32 m0, s19, 0x2000
	s_add_i32 s20, s20, s18
	global_load_lds_dwordx4 v255, s[16:17]
	s_add_i32 m0, s20, 0xc000
	s_add_u32 s16, s16, 0x20000
	global_load_lds_dwordx4 v194, s[14:15]
	s_addc_u32 s17, s17, 0
	s_add_u32 s14, s14, 0x20000
	s_addc_u32 s15, s15, 0
	s_waitcnt lgkmcnt(7)
	v_mfma_f32_32x32x16_bf16 v[96:111], v[112:115], v[162:165], v[80:95]
	v_exp_f32_e32 v208, v152
	v_exp_f32_e32 v209, v153
	v_add_f32_e32 v152, v128, v129
	v_add_f32_e32 v153, v130, v131
	v_exp_f32_e32 v210, v154
	v_add_f32_e32 v152, v152, v153
	v_add_f32_e32 v153, v132, v133
	v_add_f32_e32 v154, v134, v135
	v_exp_f32_e32 v211, v155
	s_waitcnt lgkmcnt(6)
	v_mfma_f32_32x32x16_bf16 v[96:111], v[116:119], v[166:169], v[96:111]
	v_add_f32_e32 v153, v153, v154
	v_add_f32_e32 v154, v136, v137
	v_add_f32_e32 v155, v138, v139
	v_add_f32_e32 v154, v154, v155
	v_add_f32_e32 v155, v140, v141
	s_waitcnt lgkmcnt(5)
	v_mfma_f32_32x32x16_bf16 v[96:111], v[120:123], v[170:173], v[96:111]
	v_exp_f32_e32 v156, v156
	v_exp_f32_e32 v157, v157
	v_exp_f32_e32 v158, v158
	v_exp_f32_e32 v159, v159
	s_waitcnt lgkmcnt(4)
	v_mfma_f32_32x32x16_bf16 v[96:111], v[124:127], v[174:177], v[96:111]
	s_waitcnt lgkmcnt(3)
	v_mfma_f32_32x32x16_bf16 v[112:127], v[190:193], v[162:165], v[80:95]
	v_add_f32_e32 v190, v142, v143
	v_add_f32_e32 v155, v155, v190
	v_add_f32_e32 v190, v144, v145
	v_add_f32_e32 v191, v146, v147
	v_add_f32_e32 v190, v190, v191
	v_add_f32_e32 v152, v152, v190
	v_add_f32_e32 v190, v148, v149
	s_waitcnt lgkmcnt(2)
	v_mfma_f32_32x32x16_bf16 v[112:127], v[202:205], v[166:169], v[112:127]
	v_lshl_add_u32 v205, s42, 14, v217
	ds_read_b64_tr_b16 v[64:65], v205 offset:0
	ds_read_b64_tr_b16 v[66:67], v205 offset:0x800
	ds_read_b64_tr_b16 v[68:69], v205 offset:0x1000
	ds_read_b64_tr_b16 v[70:71], v205 offset:0x1800
	ds_read_b64_tr_b16 v[72:73], v205 offset:0x2000
	ds_read_b64_tr_b16 v[74:75], v205 offset:0x2800
	ds_read_b64_tr_b16 v[76:77], v205 offset:0x3000
	ds_read_b64_tr_b16 v[78:79], v205 offset:0x3800
	v_add_f32_e32 v191, v150, v151
	v_add_f32_e32 v190, v190, v191
	v_add_f32_e32 v153, v153, v190
	v_add_f32_e32 v190, v208, v209
	v_add_f32_e32 v191, v210, v211
	v_add_f32_e32 v190, v190, v191
	v_add_f32_e32 v154, v154, v190
	s_waitcnt lgkmcnt(9)
	v_mfma_f32_32x32x16_bf16 v[112:127], v[234:237], v[170:173], v[112:127]
	v_add_f32_e32 v190, v156, v157
	v_add_f32_e32 v191, v158, v159
	v_add_f32_e32 v190, v190, v191
	v_add_f32_e32 v155, v155, v190
	v_add_f32_e32 v152, v152, v153
	v_add_f32_e32 v153, v154, v155
	v_add_f32_e32 v203, v152, v153
	s_waitcnt lgkmcnt(8)
	v_mfma_f32_32x32x16_bf16 v[112:127], v[238:241], v[174:177], v[112:127]
	v_mov_b32_e32 v204, v203
	v_cvt_pk_bf16_f32 v152, v128, v129
	v_cvt_pk_bf16_f32 v153, v130, v131
	v_cvt_pk_bf16_f32 v154, v132, v133
	v_cvt_pk_bf16_f32 v155, v134, v135
	v_cvt_pk_bf16_f32 v136, v136, v137
	v_cvt_pk_bf16_f32 v137, v138, v139
	v_cvt_pk_bf16_f32 v138, v140, v141
	v_cvt_pk_bf16_f32 v139, v142, v143
	v_permlane32_swap_b32_e32 v152, v154
	v_permlane32_swap_b32_e32 v153, v155
	v_cvt_pk_bf16_f32 v132, v144, v145
	v_cvt_pk_bf16_f32 v133, v146, v147
	v_cvt_pk_bf16_f32 v134, v148, v149
	v_cvt_pk_bf16_f32 v135, v150, v151
	s_waitcnt lgkmcnt(0)
	v_mfma_f32_32x32x16_bf16 v[0:15], v[152:155], v[64:67], v[0:15]
	v_permlane32_swap_b32_e32 v136, v138
	v_permlane32_swap_b32_e32 v137, v139
	v_cvt_pk_bf16_f32 v128, v208, v209
	v_cvt_pk_bf16_f32 v129, v210, v211
	v_cvt_pk_bf16_f32 v130, v156, v157
	v_cvt_pk_bf16_f32 v131, v158, v159
	v_mfma_f32_32x32x16_bf16 v[0:15], v[136:139], v[68:71], v[0:15]
	v_permlane32_swap_b32_e32 v132, v134
	v_permlane32_swap_b32_e32 v133, v135
	ds_read_b64_tr_b16 v[190:191], v205 offset:0x200
	ds_read_b64_tr_b16 v[192:193], v205 offset:0xa00
	ds_read_b64_tr_b16 v[234:235], v205 offset:0x1200
	ds_read_b64_tr_b16 v[236:237], v205 offset:0x1a00
	ds_read_b64_tr_b16 v[238:239], v205 offset:0x2200
	ds_read_b64_tr_b16 v[240:241], v205 offset:0x2a00
	ds_read_b64_tr_b16 v[242:243], v205 offset:0x3200
	ds_read_b64_tr_b16 v[244:245], v205 offset:0x3a00
	v_mfma_f32_32x32x16_bf16 v[0:15], v[132:135], v[72:75], v[0:15]
	v_permlane32_swap_b32_e32 v128, v130
	v_permlane32_swap_b32_e32 v129, v131
	v_permlane32_swap_b32_e32 v203, v204
	v_max_f32_e32 v140, v96, v97
	v_max3_f32 v140, v140, v112, v114
	v_max3_f32 v141, v98, v99, v113
	v_max3_f32 v140, v140, v115, v100
	v_max3_f32 v141, v141, v102, v103
	v_mfma_f32_32x32x16_bf16 v[0:15], v[128:131], v[76:79], v[0:15]
	v_max3_f32 v202, v140, v101, v116
	v_max3_f32 v208, v141, v118, v119
	ds_read_b64_tr_b16 v[156:157], v205 offset:0x400
	ds_read_b64_tr_b16 v[158:159], v205 offset:0xc00
	ds_read_b64_tr_b16 v[148:149], v205 offset:0x1400
	ds_read_b64_tr_b16 v[150:151], v205 offset:0x1c00
	ds_read_b64_tr_b16 v[144:145], v205 offset:0x2400
	ds_read_b64_tr_b16 v[146:147], v205 offset:0x2c00
	ds_read_b64_tr_b16 v[140:141], v205 offset:0x3400
	ds_read_b64_tr_b16 v[142:143], v205 offset:0x3c00
	s_waitcnt lgkmcnt(8)
	v_mfma_f32_32x32x16_bf16 v[48:63], v[152:155], v[190:193], v[48:63]
	v_max3_f32 v190, v202, v117, v104
	v_max3_f32 v191, v208, v106, v107
	v_max3_f32 v190, v190, v105, v120
	v_max3_f32 v191, v191, v122, v123
	v_max3_f32 v190, v190, v121, v108
	v_max3_f32 v191, v191, v110, v111
	v_max3_f32 v190, v190, v109, v124
	v_mfma_f32_32x32x16_bf16 v[48:63], v[136:139], v[234:237], v[48:63]
	v_max3_f32 v191, v191, v126, v127
	v_max3_f32 v190, v190, v125, v191
	v_mov_b32_e32 v191, v190
	s_nop 1
	v_permlane32_swap_b32_e32 v190, v191
	v_mfma_f32_32x32x16_bf16 v[48:63], v[132:135], v[238:241], v[48:63]
	v_max_f32_e32 v234, v190, v191
	s_mov_b32 s2, 0x4138aa3b
	v_cmp_ge_f32_e32 vcc, s2, v234
	v_mfma_f32_32x32x16_bf16 v[48:63], v[128:131], v[242:245], v[48:63]
	s_cmp_eq_u64 vcc, exec
	v_mov_b32_e32 v202, 1.0
	s_cbranch_scc0 .LBB0_837

; __device__ __forceinline__ void qkt64c(f32x16& p0, f32x16& p1, const char* Ks, const bf16x8* qr, const f32x16& cinit, int r32, int hi) {
; #pragma unroll
;     for (int d0 = 0; d0 < 4; ++d0) { const int cb = (d0 * 16 + hi * 8) * 2;
;         const bf16x8 b0 = *reinterpret_cast<const bf16x8*>(Ks + kswz<64>(r32, cb));
;         const bf16x8 b1 = *reinterpret_cast<const bf16x8*>(Ks + kswz<64>(32 + r32, cb));
;         if (d0 == 0) { p0 = __builtin_amdgcn_mfma_f32_32x32x16_bf16(b0, qr[0], cinit, 0, 0, 0); p1 = __builtin_amdgcn_mfma_f32_32x32x16_bf16(b1, qr[0], cinit, 0, 0, 0); }
;         else { p0 = __builtin_amdgcn_mfma_f32_32x32x16_bf16(b0, qr[d0], p0, 0, 0, 0); p1 = __builtin_amdgcn_mfma_f32_32x32x16_bf16(b1, qr[d0], p1, 0, 0, 0); } }
; }
.Latt9_p2_top:
	ds_read_b128 v[144:147], v128 offset:49152
	ds_read_b128 v[148:151], v129 offset:49152
	ds_read_b128 v[152:155], v130 offset:49152
	ds_read_b128 v[156:159], v131 offset:49152
	ds_read_b128 v[190:193], v128 offset:53248
	ds_read_b128 v[236:239], v129 offset:53248
	ds_read_b128 v[240:243], v130 offset:53248
	ds_read_b128 v[244:247], v131 offset:53248
	s_lshl_b32 s19, s29, 14
	s_add_i32 s19, s19, s18
	s_mov_b32 m0, s19
	s_lshl_b32 s20, s29, 13
	global_load_lds_dwordx4 v195, s[16:17]
	s_add_i32 m0, s19, 0x2000
	s_add_i32 s20, s20, s18
	global_load_lds_dwordx4 v255, s[16:17]
	s_add_i32 m0, s20, 0xc000
	s_add_u32 s16, s16, 0x20000
	global_load_lds_dwordx4 v194, s[14:15]
	s_addc_u32 s17, s17, 0
	s_add_u32 s14, s14, 0x20000
	s_addc_u32 s15, s15, 0
	s_waitcnt lgkmcnt(7)
	v_mfma_f32_32x32x16_bf16 v[128:143], v[144:147], v[162:165], v[80:95]
	v_exp_f32_e32 v208, v120
	v_exp_f32_e32 v209, v121
	v_add_f32_e32 v120, v96, v97
	v_add_f32_e32 v121, v98, v99
	v_exp_f32_e32 v210, v122
	v_add_f32_e32 v120, v120, v121
	v_add_f32_e32 v121, v100, v101
	v_add_f32_e32 v122, v102, v103
	v_exp_f32_e32 v211, v123
	s_waitcnt lgkmcnt(6)
	v_mfma_f32_32x32x16_bf16 v[128:143], v[148:151], v[166:169], v[128:143]
	v_add_f32_e32 v121, v121, v122
	v_add_f32_e32 v122, v104, v105
	v_add_f32_e32 v123, v106, v107
	v_add_f32_e32 v122, v122, v123
	v_add_f32_e32 v123, v108, v109
	s_waitcnt lgkmcnt(5)
	v_mfma_f32_32x32x16_bf16 v[128:143], v[152:155], v[170:173], v[128:143]
	v_exp_f32_e32 v124, v124
	v_exp_f32_e32 v125, v125
	v_exp_f32_e32 v126, v126
	v_exp_f32_e32 v127, v127
	v_cvt_pk_bf16_f32 v96, v96, v97
	s_waitcnt lgkmcnt(4)
	v_mfma_f32_32x32x16_bf16 v[128:143], v[156:159], v[174:177], v[128:143]
	v_cvt_pk_bf16_f32 v97, v98, v99
	v_cvt_pk_bf16_f32 v98, v100, v101
	v_cvt_pk_bf16_f32 v99, v102, v103
	s_nop 0
	v_permlane32_swap_b32_e32 v96, v98
	s_waitcnt lgkmcnt(3)
	v_mfma_f32_32x32x16_bf16 v[144:159], v[190:193], v[162:165], v[80:95]
	v_add_f32_e32 v190, v110, v111
	v_add_f32_e32 v123, v123, v190
	v_add_f32_e32 v190, v112, v113
	v_add_f32_e32 v191, v114, v115
	v_add_f32_e32 v190, v190, v191
	v_add_f32_e32 v120, v190, v120
	v_add_f32_e32 v190, v116, v117
	s_waitcnt lgkmcnt(2)
	v_mfma_f32_32x32x16_bf16 v[144:159], v[236:239], v[166:169], v[144:159]
	v_lshl_add_u32 v238, s12, 14, v221
	ds_read_b64_tr_b16 v[64:65], v238 offset:0
	ds_read_b64_tr_b16 v[66:67], v238 offset:0x800
	ds_read_b64_tr_b16 v[68:69], v238 offset:0x1000
	ds_read_b64_tr_b16 v[70:71], v238 offset:0x1800
	ds_read_b64_tr_b16 v[72:73], v238 offset:0x2000
	ds_read_b64_tr_b16 v[74:75], v238 offset:0x2800
	ds_read_b64_tr_b16 v[76:77], v238 offset:0x3000
	ds_read_b64_tr_b16 v[78:79], v238 offset:0x3800
	v_add_f32_e32 v191, v118, v119
	v_add_f32_e32 v190, v190, v191
	v_add_f32_e32 v121, v190, v121
	v_add_f32_e32 v190, v208, v209
	v_add_f32_e32 v191, v210, v211
	v_add_f32_e32 v190, v190, v191
	v_add_f32_e32 v122, v122, v190
	s_waitcnt lgkmcnt(9)
	v_mfma_f32_32x32x16_bf16 v[144:159], v[240:243], v[170:173], v[144:159]
	v_add_f32_e32 v190, v124, v125
	v_add_f32_e32 v191, v126, v127
	v_add_f32_e32 v190, v190, v191
	v_add_f32_e32 v123, v123, v190
	v_add_f32_e32 v120, v120, v121
	v_add_f32_e32 v121, v122, v123
	v_add_f32_e32 v235, v120, v121
	s_waitcnt lgkmcnt(8)
	v_mfma_f32_32x32x16_bf16 v[144:159], v[244:247], v[174:177], v[144:159]
	v_mov_b32_e32 v236, v235
	v_cvt_pk_bf16_f32 v120, v104, v105
	v_cvt_pk_bf16_f32 v121, v106, v107
	v_cvt_pk_bf16_f32 v122, v108, v109
	v_cvt_pk_bf16_f32 v123, v110, v111
	v_permlane32_swap_b32_e32 v97, v99
	v_cvt_pk_bf16_f32 v104, v112, v113
	v_cvt_pk_bf16_f32 v105, v114, v115
	v_cvt_pk_bf16_f32 v106, v116, v117
	v_cvt_pk_bf16_f32 v107, v118, v119
	s_waitcnt lgkmcnt(0)
	v_mfma_f32_32x32x16_bf16 v[0:15], v[96:99], v[64:67], v[0:15]
	v_permlane32_swap_b32_e32 v120, v122
	v_permlane32_swap_b32_e32 v121, v123
	v_cvt_pk_bf16_f32 v100, v208, v209
	v_cvt_pk_bf16_f32 v101, v210, v211
	v_cvt_pk_bf16_f32 v102, v124, v125
	v_cvt_pk_bf16_f32 v103, v126, v127
	v_mfma_f32_32x32x16_bf16 v[0:15], v[120:123], v[68:71], v[0:15]
	v_permlane32_swap_b32_e32 v104, v106
	v_permlane32_swap_b32_e32 v105, v107
	ds_read_b64_tr_b16 v[190:191], v238 offset:0x200
	ds_read_b64_tr_b16 v[192:193], v238 offset:0xa00
	ds_read_b64_tr_b16 v[240:241], v238 offset:0x1200
	ds_read_b64_tr_b16 v[242:243], v238 offset:0x1a00
	ds_read_b64_tr_b16 v[244:245], v238 offset:0x2200
	ds_read_b64_tr_b16 v[246:247], v238 offset:0x2a00
	ds_read_b64_tr_b16 v[208:209], v238 offset:0x3200
	ds_read_b64_tr_b16 v[210:211], v238 offset:0x3a00
	v_mfma_f32_32x32x16_bf16 v[0:15], v[104:107], v[72:75], v[0:15]
	v_permlane32_swap_b32_e32 v100, v102
	v_permlane32_swap_b32_e32 v101, v103
	v_permlane32_swap_b32_e32 v235, v236
	v_max_f32_e32 v108, v128, v129
	v_max3_f32 v108, v108, v144, v146
	v_max3_f32 v109, v130, v131, v145
	v_max3_f32 v108, v108, v147, v132
	v_max3_f32 v109, v109, v134, v135
	v_mfma_f32_32x32x16_bf16 v[0:15], v[100:103], v[76:79], v[0:15]
	v_max3_f32 v237, v108, v133, v148
	v_max3_f32 v239, v109, v150, v151
	ds_read_b64_tr_b16 v[124:125], v238 offset:0x400
	ds_read_b64_tr_b16 v[126:127], v238 offset:0xc00
	ds_read_b64_tr_b16 v[116:117], v238 offset:0x1400
	ds_read_b64_tr_b16 v[118:119], v238 offset:0x1c00
	ds_read_b64_tr_b16 v[112:113], v238 offset:0x2400
	ds_read_b64_tr_b16 v[114:115], v238 offset:0x2c00
	ds_read_b64_tr_b16 v[108:109], v238 offset:0x3400
	ds_read_b64_tr_b16 v[110:111], v238 offset:0x3c00
	s_waitcnt lgkmcnt(8)
	v_mfma_f32_32x32x16_bf16 v[48:63], v[96:99], v[190:193], v[48:63]
	v_max3_f32 v190, v237, v149, v136
	v_max3_f32 v191, v239, v138, v139
	v_max3_f32 v190, v190, v137, v152
	v_max3_f32 v191, v191, v154, v155
	v_max3_f32 v190, v190, v153, v140
	v_max3_f32 v191, v191, v142, v143
	v_max3_f32 v190, v190, v141, v156
	v_mfma_f32_32x32x16_bf16 v[48:63], v[120:123], v[240:243], v[48:63]
	v_max3_f32 v191, v191, v158, v159
	v_max3_f32 v190, v190, v157, v191
	v_mov_b32_e32 v191, v190
	s_nop 1
	v_permlane32_swap_b32_e32 v190, v191
	v_mfma_f32_32x32x16_bf16 v[48:63], v[104:107], v[244:247], v[48:63]
	v_max_f32_e32 v237, v190, v191
	s_mov_b32 s2, 0x4138aa3b
	v_cmp_ge_f32_e32 vcc, s2, v237
	v_mfma_f32_32x32x16_bf16 v[48:63], v[100:103], v[208:211], v[48:63]
	s_cmp_eq_u64 vcc, exec
	s_cbranch_scc0 .LBB0_859
	v_mov_b32_e32 v237, 1.0

; __device__ __forceinline__ void qkt64c(f32x16& p0, f32x16& p1, const char* Ks, const bf16x8* qr, const f32x16& cinit, int r32, int hi) {
; #pragma unroll
;     for (int d0 = 0; d0 < 4; ++d0) { const int cb = (d0 * 16 + hi * 8) * 2;
;         const bf16x8 b0 = *reinterpret_cast<const bf16x8*>(Ks + kswz<64>(r32, cb));
;         const bf16x8 b1 = *reinterpret_cast<const bf16x8*>(Ks + kswz<64>(32 + r32, cb));
;         if (d0 == 0) { p0 = __builtin_amdgcn_mfma_f32_32x32x16_bf16(b0, qr[0], cinit, 0, 0, 0); p1 = __builtin_amdgcn_mfma_f32_32x32x16_bf16(b1, qr[0], cinit, 0, 0, 0); }
;         else { p0 = __builtin_amdgcn_mfma_f32_32x32x16_bf16(b0, qr[d0], p0, 0, 0, 0); p1 = __builtin_amdgcn_mfma_f32_32x32x16_bf16(b1, qr[d0], p1, 0, 0, 0); } }
; }
.LBB0_852:
	s_waitcnt lgkmcnt(0)
	v_add_u32_e32 v102, s2, v227
	v_add_u32_e32 v103, s2, v231
	v_add_u32_e32 v104, s2, v232
	v_add_u32_e32 v105, s2, v233
	s_waitcnt vmcnt(0)
	s_barrier
	ds_read_b128 v[112:115], v102 offset:49152
	ds_read_b128 v[116:119], v103 offset:49152
	ds_read_b128 v[120:123], v104 offset:49152
	ds_read_b128 v[124:127], v105 offset:49152
	ds_read_b128 v[190:193], v102 offset:53248
	ds_read_b128 v[202:205], v103 offset:53248
	ds_read_b128 v[208:211], v104 offset:53248
	ds_read_b128 v[238:241], v105 offset:53248
	s_add_i32 s3, s29, 1
	s_cmp_lg_u32 s29, 2
	s_cselect_b32 s3, s3, 0
	s_lshl_b32 s19, s3, 14
	s_add_i32 s19, s19, s18
	s_mov_b32 m0, s19
	s_lshl_b32 s20, s3, 13
	global_load_lds_dwordx4 v195, s[16:17]
	s_add_i32 m0, s19, 0x2000
	s_add_i32 s20, s20, s18
	global_load_lds_dwordx4 v255, s[16:17]
	s_add_i32 m0, s20, 0xc000
	s_add_u32 s16, s16, 0x20000
	global_load_lds_dwordx4 v194, s[14:15]
	s_addc_u32 s17, s17, 0
	s_add_u32 s14, s14, 0x20000
	s_addc_u32 s15, s15, 0
	s_waitcnt lgkmcnt(7)
	v_mfma_f32_32x32x16_bf16 v[96:111], v[112:115], v[162:165], v[80:95]
	v_exp_f32_e32 v242, v152
	v_exp_f32_e32 v243, v153
	v_add_f32_e32 v152, v128, v129
	v_add_f32_e32 v153, v130, v131
	v_exp_f32_e32 v244, v154
	v_add_f32_e32 v152, v152, v153
	v_add_f32_e32 v153, v132, v133
	v_add_f32_e32 v154, v134, v135
	v_exp_f32_e32 v245, v155
	s_waitcnt lgkmcnt(6)
	v_mfma_f32_32x32x16_bf16 v[96:111], v[116:119], v[166:169], v[96:111]
	v_add_f32_e32 v153, v153, v154
	v_add_f32_e32 v154, v136, v137
	v_add_f32_e32 v155, v138, v139
	v_add_f32_e32 v154, v154, v155
	v_add_f32_e32 v155, v140, v141
	s_waitcnt lgkmcnt(5)
	v_mfma_f32_32x32x16_bf16 v[96:111], v[120:123], v[170:173], v[96:111]
	v_exp_f32_e32 v156, v156
	v_exp_f32_e32 v157, v157
	v_exp_f32_e32 v158, v158
	v_exp_f32_e32 v159, v159
	s_waitcnt lgkmcnt(4)
	v_mfma_f32_32x32x16_bf16 v[96:111], v[124:127], v[174:177], v[96:111]
	s_waitcnt lgkmcnt(3)
	v_mfma_f32_32x32x16_bf16 v[112:127], v[190:193], v[162:165], v[80:95]
	v_add_f32_e32 v190, v142, v143
	v_add_f32_e32 v155, v155, v190
	v_add_f32_e32 v190, v144, v145
	v_add_f32_e32 v191, v146, v147
	v_add_f32_e32 v190, v190, v191
	v_add_f32_e32 v152, v152, v190
	v_add_f32_e32 v190, v148, v149
	s_waitcnt lgkmcnt(2)
	v_mfma_f32_32x32x16_bf16 v[112:127], v[202:205], v[166:169], v[112:127]
	v_lshl_add_u32 v205, s30, 14, v221
	ds_read_b64_tr_b16 v[64:65], v205 offset:0
	ds_read_b64_tr_b16 v[66:67], v205 offset:0x800
	ds_read_b64_tr_b16 v[68:69], v205 offset:0x1000
	ds_read_b64_tr_b16 v[70:71], v205 offset:0x1800
	ds_read_b64_tr_b16 v[72:73], v205 offset:0x2000
	ds_read_b64_tr_b16 v[74:75], v205 offset:0x2800
	ds_read_b64_tr_b16 v[76:77], v205 offset:0x3000
	ds_read_b64_tr_b16 v[78:79], v205 offset:0x3800
	v_add_f32_e32 v191, v150, v151
	v_add_f32_e32 v190, v190, v191
	v_add_f32_e32 v153, v153, v190
	v_add_f32_e32 v190, v242, v243
	v_add_f32_e32 v191, v244, v245
	v_add_f32_e32 v190, v190, v191
	v_add_f32_e32 v154, v154, v190
	s_waitcnt lgkmcnt(9)
	v_mfma_f32_32x32x16_bf16 v[112:127], v[208:211], v[170:173], v[112:127]
	v_add_f32_e32 v190, v156, v157
	v_add_f32_e32 v191, v158, v159
	v_add_f32_e32 v190, v190, v191
	v_add_f32_e32 v155, v155, v190
	v_add_f32_e32 v152, v152, v153
	v_add_f32_e32 v153, v154, v155
	v_add_f32_e32 v203, v152, v153
	s_waitcnt lgkmcnt(8)
	v_mfma_f32_32x32x16_bf16 v[112:127], v[238:241], v[174:177], v[112:127]
	v_mov_b32_e32 v204, v203
	v_cvt_pk_bf16_f32 v152, v128, v129
	v_cvt_pk_bf16_f32 v153, v130, v131
	v_cvt_pk_bf16_f32 v154, v132, v133
	v_cvt_pk_bf16_f32 v155, v134, v135
	v_cvt_pk_bf16_f32 v136, v136, v137
	v_cvt_pk_bf16_f32 v137, v138, v139
	v_cvt_pk_bf16_f32 v138, v140, v141
	v_cvt_pk_bf16_f32 v139, v142, v143
	v_permlane32_swap_b32_e32 v152, v154
	v_permlane32_swap_b32_e32 v153, v155
	v_cvt_pk_bf16_f32 v132, v144, v145
	v_cvt_pk_bf16_f32 v133, v146, v147
	v_cvt_pk_bf16_f32 v134, v148, v149
	v_cvt_pk_bf16_f32 v135, v150, v151
	s_waitcnt lgkmcnt(0)
	v_mfma_f32_32x32x16_bf16 v[0:15], v[152:155], v[64:67], v[0:15]
	v_permlane32_swap_b32_e32 v136, v138
	v_permlane32_swap_b32_e32 v137, v139
	v_cvt_pk_bf16_f32 v128, v242, v243
	v_cvt_pk_bf16_f32 v129, v244, v245
	v_cvt_pk_bf16_f32 v130, v156, v157
	v_cvt_pk_bf16_f32 v131, v158, v159
	v_mfma_f32_32x32x16_bf16 v[0:15], v[136:139], v[68:71], v[0:15]
	v_permlane32_swap_b32_e32 v132, v134
	v_permlane32_swap_b32_e32 v133, v135
	ds_read_b64_tr_b16 v[190:191], v205 offset:0x200
	ds_read_b64_tr_b16 v[192:193], v205 offset:0xa00
	ds_read_b64_tr_b16 v[208:209], v205 offset:0x1200
	ds_read_b64_tr_b16 v[210:211], v205 offset:0x1a00
	ds_read_b64_tr_b16 v[238:239], v205 offset:0x2200
	ds_read_b64_tr_b16 v[240:241], v205 offset:0x2a00
	ds_read_b64_tr_b16 v[242:243], v205 offset:0x3200
	ds_read_b64_tr_b16 v[244:245], v205 offset:0x3a00
	v_mfma_f32_32x32x16_bf16 v[0:15], v[132:135], v[72:75], v[0:15]
	v_permlane32_swap_b32_e32 v128, v130
	v_permlane32_swap_b32_e32 v129, v131
	v_permlane32_swap_b32_e32 v203, v204
	v_max_f32_e32 v140, v96, v97
	v_max3_f32 v140, v140, v112, v114
	v_max3_f32 v141, v98, v99, v113
	v_max3_f32 v140, v140, v115, v100
	v_max3_f32 v141, v141, v102, v103
	v_mfma_f32_32x32x16_bf16 v[0:15], v[128:131], v[76:79], v[0:15]
	v_max3_f32 v202, v140, v101, v116
	v_max3_f32 v246, v141, v118, v119
	ds_read_b64_tr_b16 v[156:157], v205 offset:0x400
	ds_read_b64_tr_b16 v[158:159], v205 offset:0xc00
	ds_read_b64_tr_b16 v[148:149], v205 offset:0x1400
	ds_read_b64_tr_b16 v[150:151], v205 offset:0x1c00
	ds_read_b64_tr_b16 v[144:145], v205 offset:0x2400
	ds_read_b64_tr_b16 v[146:147], v205 offset:0x2c00
	ds_read_b64_tr_b16 v[140:141], v205 offset:0x3400
	ds_read_b64_tr_b16 v[142:143], v205 offset:0x3c00
	s_waitcnt lgkmcnt(8)
	v_mfma_f32_32x32x16_bf16 v[48:63], v[152:155], v[190:193], v[48:63]
	v_max3_f32 v190, v202, v117, v104
	v_max3_f32 v191, v246, v106, v107
	v_max3_f32 v190, v190, v105, v120
	v_max3_f32 v191, v191, v122, v123
	v_max3_f32 v190, v190, v121, v108
	v_max3_f32 v191, v191, v110, v111
	v_max3_f32 v190, v190, v109, v124
	v_mfma_f32_32x32x16_bf16 v[48:63], v[136:139], v[208:211], v[48:63]
	v_max3_f32 v191, v191, v126, v127
	v_max3_f32 v190, v190, v125, v191
	v_mov_b32_e32 v191, v190
	s_nop 1
	v_permlane32_swap_b32_e32 v190, v191
	v_mfma_f32_32x32x16_bf16 v[48:63], v[132:135], v[238:241], v[48:63]
	v_max_f32_e32 v238, v190, v191
	s_mov_b32 s2, 0x4138aa3b
	v_cmp_ge_f32_e32 vcc, s2, v238
	v_mfma_f32_32x32x16_bf16 v[48:63], v[128:131], v[242:245], v[48:63]
	s_cmp_eq_u64 vcc, exec
	v_mov_b32_e32 v202, 1.0
	s_cbranch_scc0 .LBB0_860
